# v12: hand-written router row body + 192 router / 64 sweeper workgroups
# speedup vs baseline: 1.0496x; 1.0066x over previous
; #define LAS __attribute__((address_space(3)))
; __device__ __forceinline__ void phase_router(const Ctx& P, LAS unsigned char* lds, int vcu, int G) {
;     const int tid = threadIdx.x, lane = tid & 63, wave = __builtin_amdgcn_readfirstlane(tid >> 6);
;     LAS float* rwT = (LAS float*)lds;
;     LAS unsigned char* rows8 = lds + 65536;
;     LAS int* sel = (LAS int*)(lds + LDS_MISC + 1024);
;     LAS float* prb = (LAS float*)(lds + LDS_MISC + 1024 + 256);
;     LAS int* lrank = (LAS int*)(lds + LDS_MISC + 1024 + 512);
;     LAS int* lcnt = (LAS int*)(lds + LDS_MISC + 1024 + 768);
;     LAS int* lbase = (LAS int*)(lds + LDS_MISC + 1024 + 832);
;     LAS float* rscl = (LAS float*)(lds + LDS_MISC + 1024 + 864);
;     for (int i = tid; i < DM * 8; i += 512) { const int k = i >> 3, e = i & 7; rwT[e * DM + k] = P.in[29][i]; }
;     __syncthreads();
;     const float* mod = (const float*)(P.ws + WS_MOD) + (size_t)5 * NMOD;
;     const float* gvec = P.in[7] + DM;
;     unsigned char* HNP = P.ws + WS_HNP; unsigned* ecnt = (unsigned*)(P.ws + WS_CTL) + CW_ECNT; int* tok = (int*)(P.ws + WS_TOK);
;     for (int blk = vcu; blk < ML / 32; blk += G) {
;         if (tid < 8) lcnt[tid] = 0;
;         for (int q = 0; q < 4; ++q) {
.LBB0_2342:
	s_or_b64 exec, exec, s[2:3]
	v_and_b32_e32 v1, 63, v0
	v_readfirstlane_b32 s12, v0
	s_cmpk_gt_i32 s33, 0x1ff
	v_lshlrev_b32_e32 v74, 2, v1
	s_waitcnt lgkmcnt(0)
	s_barrier
	s_cbranch_scc1 .LBB0_2377
	v_mov_b64_e32 v[2:3], s[28:29]
	flat_load_dwordx2 v[2:3], v[2:3] offset:56
	s_add_u32 s9, s36, 0x13c000
	v_mov_b32_e32 v11, 0
	v_mbcnt_lo_u32_b32 v7, -1, 0
	v_lshlrev_b32_e32 v10, 8, v0
	s_addc_u32 s38, s37, 0
	s_mov_b64 s[14:15], 0x4000
	v_mbcnt_hi_u32_b32 v7, -1, v7
	v_lshl_add_u64 v[12:13], s[36:37], 0, v[10:11]
	s_add_u32 s30, s36, 0x200000
	v_and_b32_e32 v9, 64, v7
	v_lshl_add_u64 v[12:13], v[12:13], 0, s[14:15]
	s_addc_u32 s31, s37, 0
	s_lshr_b32 s14, s12, 4
	v_xor_b32_e32 v14, 1, v7
	s_add_i32 s13, 0, 0x20700
	v_add_u32_e32 v9, 64, v9
	s_and_b32 s46, s14, 0xffffffc
	v_lshlrev_b32_e32 v5, 2, v0
	v_xor_b32_e32 v15, 2, v7
	v_cmp_lt_i32_e32 vcc, v14, v9
	s_add_u32 s47, s36, 0x1c2c0000
	v_add_u32_e32 v62, s13, v5
	v_cndmask_b32_e32 v14, v7, v14, vcc
	v_cmp_lt_i32_e32 vcc, v15, v9
	s_addc_u32 s48, s37, 0
	s_add_i32 s72, 0, 0x20600
	s_add_i32 s71, 0, 0x20400
	s_add_i32 s13, 0, 0x20740
	s_add_i32 s15, 0, 0x20500
	s_mov_b64 s[10:11], 0x2000
	v_cndmask_b32_e32 v15, v7, v15, vcc
	s_add_u32 s34, s36, 0x5cf30000
	v_lshlrev_b32_e32 v63, 2, v14
	v_lshlrev_b32_e32 v64, 2, v15
	s_addc_u32 s35, s37, 0
	s_add_i32 s76, 0, 0x10000
	s_add_i32 s68, 0, 0x20760
	v_xor_b32_e32 v16, 4, v7
	v_lshlrev_b32_e32 v10, 4, v1
	v_xor_b32_e32 v17, 8, v7
	v_cmp_lt_i32_e32 vcc, v16, v9
	v_add_u32_e32 v69, s72, v5
	v_add_u32_e32 v70, s71, v5
	v_xor_b32_e32 v25, 16, v7
	v_cndmask_b32_e32 v16, v7, v16, vcc
	v_cmp_lt_i32_e32 vcc, v17, v9
	v_lshl_add_u64 v[32:33], s[36:37], 0, v[10:11]
	v_xor_b32_e32 v26, 32, v7
	v_cndmask_b32_e32 v17, v7, v17, vcc
	v_cmp_lt_i32_e32 vcc, v25, v9
	v_or_b32_e32 v4, 0x100, v74
	v_or_b32_e32 v6, 0x200, v74
	v_or_b32_e32 v8, 0x300, v74
	v_or_b32_e32 v34, 0x400, v74
	v_cndmask_b32_e32 v25, v7, v25, vcc
	v_cmp_lt_i32_e32 vcc, v26, v9
	v_or_b32_e32 v36, 0x600, v74
	v_or_b32_e32 v38, 0x700, v74
	v_and_b32_e32 v58, 1, v0
	v_lshlrev_b32_e32 v18, 2, v4
	v_mov_b32_e32 v19, v11
	v_lshlrev_b32_e32 v20, 2, v6
	v_mov_b32_e32 v21, v11
	v_lshlrev_b32_e32 v22, 2, v8
	v_mov_b32_e32 v23, v11
	v_lshlrev_b32_e32 v24, 2, v34
	v_cndmask_b32_e32 v7, v7, v26, vcc
	v_lshlrev_b32_e32 v67, 2, v25
	v_mov_b32_e32 v25, v11
	v_mov_b32_e32 v27, v11
	v_lshlrev_b32_e32 v28, 2, v36
	v_mov_b32_e32 v29, v11
	v_lshlrev_b32_e32 v30, 2, v38
	v_mov_b32_e32 v31, v11
	v_cmp_gt_u32_e64 s[2:3], 8, v0
	v_cmp_eq_u32_e64 s[4:5], 0, v1
	v_cmp_gt_u32_e64 s[6:7], 64, v0
	v_and_b32_e32 v59, 0xf8, v5
	v_lshlrev_b32_e32 v60, 1, v58
	s_waitcnt vmcnt(0) lgkmcnt(0)
	v_lshl_add_u64 v[14:15], v[2:3], 0, s[10:11]
	s_lshl_b32 s10, s46, 11
	s_add_i32 s49, s76, s10
	s_lshl_b32 s10, s46, 2
	s_add_i32 s50, s68, s10
	s_lshl_b32 s10, s46, 3
	s_add_i32 s51, s71, s10
	s_add_i32 s52, s72, s10
	s_or_b32 s10, s10, 4
	s_add_i32 s53, s71, s10
	s_add_i32 s54, s72, s10
	s_or_b32 s10, s46, 1
	s_lshl_b32 s11, s10, 11
	s_add_i32 s55, s76, s11
	s_lshl_b32 s11, s10, 2
	s_lshl_b32 s10, s10, 3
	s_add_i32 s57, s71, s10
	s_add_i32 s58, s72, s10
	s_or_b32 s10, s10, 4
	s_add_i32 s59, s71, s10
	s_add_i32 s60, s72, s10
	s_or_b32 s10, s46, 2
	s_add_i32 s56, s68, s11
	s_lshl_b32 s11, s10, 11
	s_add_i32 s61, s76, s11
	s_lshl_b32 s11, s10, 2
	s_lshl_b32 s10, s10, 3
	s_add_i32 s63, s71, s10
	s_add_i32 s64, s72, s10
	s_or_b32 s10, s10, 4
	s_add_i32 s65, s71, s10
	s_add_i32 s66, s72, s10
	s_or_b32 s10, s14, 3
	s_add_i32 s62, s68, s11
	s_lshl_b32 s11, s10, 11
	s_add_i32 s67, s76, s11
	s_lshl_b32 s11, s10, 2
	s_lshl_b32 s10, s10, 3
	s_add_i32 s69, s71, s10
	s_add_i32 s70, s72, s10
	s_or_b32 s10, s10, 4
	s_add_i32 s68, s68, s11
	s_add_i32 s71, s71, s10
	s_add_i32 s72, s72, s10
	s_mov_b64 s[10:11], 0x4aec0000
	s_add_u32 s73, s36, 0x1c2c0200
	v_lshl_add_u64 v[32:33], v[32:33], 0, s[10:11]
	s_addc_u32 s74, s37, 0
	s_lshr_b32 s99, s33, 2
	s_mul_i32 s99, s99, 3
	s_and_b32 s10, s33, 3
	s_add_i32 s99, s99, s10
	s_add_i32 s99, s99, -1
	s_lshl_b32 s10, s99, 5
	v_or_b32_e32 v2, 0x500, v74
	s_add_i32 s40, s10, s46
	s_lshl_b32 s10, s12, 7
	v_lshlrev_b32_e32 v26, 2, v2
	s_and_b32 s10, s10, 0xffffe000
	v_add_u32_e32 v61, 0, v10
	v_lshlrev_b32_e32 v65, 2, v16
	v_lshlrev_b32_e32 v66, 2, v17
	v_lshlrev_b32_e32 v68, 2, v7
	v_add_u32_e32 v71, s13, v5
	v_add_u32_e32 v72, s15, v5
	v_lshl_add_u64 v[16:17], v[14:15], 0, v[10:11]
	v_lshl_add_u64 v[18:19], v[14:15], 0, v[18:19]
	v_lshl_add_u64 v[20:21], v[14:15], 0, v[20:21]
	v_lshl_add_u64 v[22:23], v[14:15], 0, v[22:23]
	v_lshl_add_u64 v[24:25], v[14:15], 0, v[24:25]
	v_lshl_add_u64 v[26:27], v[14:15], 0, v[26:27]
	v_lshl_add_u64 v[28:29], v[14:15], 0, v[28:29]
	v_lshl_add_u64 v[30:31], v[14:15], 0, v[30:31]
	s_add_i32 s98, s39, 3
	s_lshr_b32 s98, s98, 2
	s_sub_i32 s98, s39, s98
	s_lshl_b32 s75, s98, 5
	s_add_i32 s76, s76, s10
	v_mov_b32_e32 v73, 0x358637bd
	v_lshlrev_b32_e32 v75, 2, v4
	v_lshlrev_b32_e32 v76, 2, v6
	v_lshlrev_b32_e32 v77, 2, v8
	v_lshlrev_b32_e32 v78, 2, v34
	v_lshlrev_b32_e32 v79, 2, v2
	v_lshlrev_b32_e32 v80, 2, v36
	v_lshlrev_b32_e32 v81, 2, v38
	s_mov_b32 s77, 0xda24260
	s_mov_b32 s78, 0x42fe0000
	s_mov_b32 s79, 0x4b3fff81
	s_mov_b32 s80, 0xc0c0400
	s_mov_b32 s81, 0x5040100
	s_mov_b32 s82, 0xff61b1e6
	v_mov_b32_e32 v82, 1
	v_mov_b32_e32 v83, 0x4b40007f
	v_mov_b32_e32 v84, 0xff61b1e6
	s_mov_b32 s83, s99
	s_branch .LBB0_2345
; __device__ __forceinline__ f32x4 ld4_bf(const bf16_t* p) { const u32x2 w = *(const u32x2*)p; return (f32x4){bf_lo(w.x), bf_hi(w.x), bf_lo(w.y), bf_hi(w.y)}; }
; __device__ __forceinline__ float sq4(const f32x4 v) { return (v[0] * v[0] + v[1] * v[1]) + (v[2] * v[2] + v[3] * v[3]); }
; __device__ __forceinline__ void phase_router(const Ctx& P, LAS unsigned char* lds, int vcu, int G) {
;     ...
;     for (int blk = vcu; blk < ML / 32; blk += G) {
;         if (tid < 8) lcnt[tid] = 0;
;         for (int q = 0; q < 4; ++q) {
;             const int lr = wave * 4 + q, row = blk * 32 + lr; const int cnd = row >> 12;
;             const bf16_t* xr = (const bf16_t*)(P.ws + WS_XA) + (size_t)row * DM;
;             f32x4 v[8]; float ss = 0.f;
; #pragma unroll
;             for (int j = 0; j < 8; ++j) { v[j] = ld4_bf(xr + 4 * lane + 256 * j); ss += sq4(v[j]); }
;             ss = wave_sum(ss); const float rstd = __builtin_amdgcn_rsqf(ss * (1.0f / DM) + EPS);
;             const float* shp = mod + (size_t)cnd * NMOD + 3 * DM; const float* scp = mod + (size_t)cnd * NMOD + 4 * DM;
;             float lg[8]; float amax = 0.f;
; #pragma unroll
;             for (int e = 0; e < 8; ++e) lg[e] = 0.f;
; #pragma unroll
;             for (int j = 0; j < 8; ++j) { const int c = 4 * lane + 256 * j; const f32x4 g4 = *(const f32x4*)(gvec + c), sc4 = *(const f32x4*)(scp + c), sh4 = *(const f32x4*)(shp + c);
;                 const f32x4 h = v[j] * rstd * g4 * (sc4 + 1.0f) + sh4;
.LBB0_2344:
	s_or_b64 exec, exec, s[10:11]
	s_add_i32 s83, s83, s98
	s_add_i32 s40, s40, s75
	s_cmpk_lt_i32 s83, 0x200
	s_barrier
	s_cbranch_scc0 .LBB0_2377
.LBB0_2345:
	s_and_saveexec_b64 s[10:11], s[2:3]
	ds_write_b32 v62, v11
	s_or_b64 exec, exec, s[10:11]
	s_ashr_i32 s41, s40, 31
	s_lshl_b64 s[10:11], s[40:41], 12
	s_add_u32 s42, s73, s10
	s_addc_u32 s43, s74, s11
	s_lshl_b32 s41, s83, 5
	s_mov_b32 s84, 0
	s_mov_b32 s85, s76
	s_lshr_b32 s12, s83, 7
	s_mul_i32 s12, s12, 0xc000
	s_add_u32 s16, s9, s12
	s_addc_u32 s17, s38, 0
	s_add_u32 s18, s16, 0x8000
	s_addc_u32 s19, s17, 0
	s_add_u32 s16, s16, 0x6000
	s_addc_u32 s17, s17, 0
	global_load_dwordx4 v[86:89], v[16:17], off
	global_load_dwordx4 v[102:105], v10, s[18:19]
	global_load_dwordx4 v[192:195], v10, s[16:17]
	global_load_dwordx4 v[90:93], v[18:19], off
	global_load_dwordx4 v[106:109], v75, s[18:19]
	global_load_dwordx4 v[196:199], v75, s[16:17]
	global_load_dwordx4 v[94:97], v[20:21], off
	global_load_dwordx4 v[110:113], v76, s[18:19]
	global_load_dwordx4 v[200:203], v76, s[16:17]
	global_load_dwordx4 v[98:101], v[22:23], off
	global_load_dwordx4 v[114:117], v77, s[18:19]
	global_load_dwordx4 v[204:207], v77, s[16:17]
	s_waitcnt vmcnt(0)
	v_pk_add_f32 v[102:103], v[102:103], 1.0 op_sel_hi:[1,0]
	v_pk_mul_f32 v[160:161], v[86:87], v[102:103]
	v_pk_add_f32 v[104:105], v[104:105], 1.0 op_sel_hi:[1,0]
	v_pk_mul_f32 v[162:163], v[88:89], v[104:105]
	v_pk_add_f32 v[106:107], v[106:107], 1.0 op_sel_hi:[1,0]
	v_pk_mul_f32 v[164:165], v[90:91], v[106:107]
	v_pk_add_f32 v[108:109], v[108:109], 1.0 op_sel_hi:[1,0]
	v_pk_mul_f32 v[166:167], v[92:93], v[108:109]
	v_pk_add_f32 v[110:111], v[110:111], 1.0 op_sel_hi:[1,0]
	v_pk_mul_f32 v[168:169], v[94:95], v[110:111]
	v_pk_add_f32 v[112:113], v[112:113], 1.0 op_sel_hi:[1,0]
	v_pk_mul_f32 v[170:171], v[96:97], v[112:113]
	v_pk_add_f32 v[114:115], v[114:115], 1.0 op_sel_hi:[1,0]
	v_pk_mul_f32 v[172:173], v[98:99], v[114:115]
	v_pk_add_f32 v[116:117], v[116:117], 1.0 op_sel_hi:[1,0]
	v_pk_mul_f32 v[174:175], v[100:101], v[116:117]
	global_load_dwordx4 v[86:89], v[24:25], off
	global_load_dwordx4 v[102:105], v78, s[18:19]
	global_load_dwordx4 v[208:211], v78, s[16:17]
	global_load_dwordx4 v[90:93], v[26:27], off
	global_load_dwordx4 v[106:109], v79, s[18:19]
	global_load_dwordx4 v[212:215], v79, s[16:17]
	global_load_dwordx4 v[94:97], v[28:29], off
	global_load_dwordx4 v[110:113], v80, s[18:19]
	global_load_dwordx4 v[216:219], v80, s[16:17]
	global_load_dwordx4 v[98:101], v[30:31], off
	global_load_dwordx4 v[114:117], v81, s[18:19]
	global_load_dwordx4 v[220:223], v81, s[16:17]
	s_waitcnt vmcnt(0)
	v_pk_add_f32 v[102:103], v[102:103], 1.0 op_sel_hi:[1,0]
	v_pk_mul_f32 v[176:177], v[86:87], v[102:103]
	v_pk_add_f32 v[104:105], v[104:105], 1.0 op_sel_hi:[1,0]
	v_pk_mul_f32 v[178:179], v[88:89], v[104:105]
	v_pk_add_f32 v[106:107], v[106:107], 1.0 op_sel_hi:[1,0]
	v_pk_mul_f32 v[180:181], v[90:91], v[106:107]
	v_pk_add_f32 v[108:109], v[108:109], 1.0 op_sel_hi:[1,0]
	v_pk_mul_f32 v[182:183], v[92:93], v[108:109]
	v_pk_add_f32 v[110:111], v[110:111], 1.0 op_sel_hi:[1,0]
	v_pk_mul_f32 v[184:185], v[94:95], v[110:111]
	v_pk_add_f32 v[112:113], v[112:113], 1.0 op_sel_hi:[1,0]
	v_pk_mul_f32 v[186:187], v[96:97], v[112:113]
	v_pk_add_f32 v[114:115], v[114:115], 1.0 op_sel_hi:[1,0]
	v_pk_mul_f32 v[188:189], v[98:99], v[114:115]
	v_pk_add_f32 v[116:117], v[116:117], 1.0 op_sel_hi:[1,0]
	v_pk_mul_f32 v[190:191], v[100:101], v[116:117]
	v_mov_b64_e32 v[2:3], s[28:29]
	flat_load_dwordx2 v[2:3], v[2:3] offset:240
	s_waitcnt vmcnt(0) lgkmcnt(0)
	global_load_dwordx4 v[224:227], v[2:3], off
	global_load_dwordx4 v[228:231], v[2:3], off offset:16
	s_waitcnt vmcnt(0)
	s_branch .LBB0_2349

; __device__ __forceinline__ f32x4 ld4_bf(const bf16_t* p) { const u32x2 w = *(const u32x2*)p; return (f32x4){bf_lo(w.x), bf_hi(w.x), bf_lo(w.y), bf_hi(w.y)}; }
; __device__ __forceinline__ float sq4(const f32x4 v) { return (v[0] * v[0] + v[1] * v[1]) + (v[2] * v[2] + v[3] * v[3]); }
; __device__ __forceinline__ void phase_router(const Ctx& P, LAS unsigned char* lds, int vcu, int G) {
;     ...
;             const int lr = wave * 4 + q, row = blk * 32 + lr; const int cnd = row >> 12;
;             const bf16_t* xr = (const bf16_t*)(P.ws + WS_XA) + (size_t)row * DM;
;             f32x4 v[8]; float ss = 0.f;
; #pragma unroll
;             for (int j = 0; j < 8; ++j) { v[j] = ld4_bf(xr + 4 * lane + 256 * j); ss += sq4(v[j]); }
;             ss = wave_sum(ss); const float rstd = __builtin_amdgcn_rsqf(ss * (1.0f / DM) + EPS);
;             const float* shp = mod + (size_t)cnd * NMOD + 3 * DM; const float* scp = mod + (size_t)cnd * NMOD + 4 * DM;
;             float lg[8]; float amax = 0.f;
; #pragma unroll
;             for (int e = 0; e < 8; ++e) lg[e] = 0.f;
; #pragma unroll
;             for (int j = 0; j < 8; ++j) { const int c = 4 * lane + 256 * j; const f32x4 g4 = *(const f32x4*)(gvec + c), sc4 = *(const f32x4*)(scp + c), sh4 = *(const f32x4*)(shp + c);
;                 const f32x4 h = v[j] * rstd * g4 * (sc4 + 1.0f) + sh4;
;                 amax = fmaxf(amax, fmaxf(fmaxf(fabsf(h[0]), fabsf(h[1])), fmaxf(fabsf(h[2]), fabsf(h[3]))));
.LBB0_2349:
	s_add_i32 s86, s84, s46
	s_add_i32 s10, s86, s41
	s_ashr_i32 s11, s10, 31
	s_lshl_b64 s[12:13], s[10:11], 12
	s_add_u32 s12, s47, s12
	s_addc_u32 s13, s48, s13
	v_lshlrev_b32_e32 v34, 1, v74
	global_load_dwordx2 v[36:37], v34, s[12:13]
	global_load_dwordx2 v[38:39], v34, s[12:13] offset:512
	global_load_dwordx2 v[40:41], v34, s[12:13] offset:1024
	global_load_dwordx2 v[42:43], v34, s[12:13] offset:1536
	global_load_dwordx2 v[44:45], v34, s[12:13] offset:2048
	global_load_dwordx2 v[46:47], v34, s[12:13] offset:2560
	global_load_dwordx2 v[48:49], v34, s[12:13] offset:3072
	global_load_dwordx2 v[50:51], v34, s[12:13] offset:3584
	v_add_u32_e32 v35, s85, v74
	s_waitcnt vmcnt(0)
	v_lshlrev_b32_e32 v86, 16, v36
	v_and_b32_e32 v87, 0xffff0000, v36
	v_lshlrev_b32_e32 v88, 16, v37
	v_and_b32_e32 v89, 0xffff0000, v37
	v_lshlrev_b32_e32 v90, 16, v38
	v_and_b32_e32 v91, 0xffff0000, v38
	v_lshlrev_b32_e32 v92, 16, v39
	v_and_b32_e32 v93, 0xffff0000, v39
	v_lshlrev_b32_e32 v94, 16, v40
	v_and_b32_e32 v95, 0xffff0000, v40
	v_lshlrev_b32_e32 v96, 16, v41
	v_and_b32_e32 v97, 0xffff0000, v41
	v_lshlrev_b32_e32 v98, 16, v42
	v_and_b32_e32 v99, 0xffff0000, v42
	v_lshlrev_b32_e32 v100, 16, v43
	v_and_b32_e32 v101, 0xffff0000, v43
	v_lshlrev_b32_e32 v102, 16, v44
	v_and_b32_e32 v103, 0xffff0000, v44
	v_lshlrev_b32_e32 v104, 16, v45
	v_and_b32_e32 v105, 0xffff0000, v45
	v_lshlrev_b32_e32 v106, 16, v46
	v_and_b32_e32 v107, 0xffff0000, v46
	v_lshlrev_b32_e32 v108, 16, v47
	v_and_b32_e32 v109, 0xffff0000, v47
	v_lshlrev_b32_e32 v110, 16, v48
	v_and_b32_e32 v111, 0xffff0000, v48
	v_lshlrev_b32_e32 v112, 16, v49
	v_and_b32_e32 v113, 0xffff0000, v49
	v_lshlrev_b32_e32 v114, 16, v50
	v_and_b32_e32 v115, 0xffff0000, v50
	v_lshlrev_b32_e32 v116, 16, v51
	v_and_b32_e32 v117, 0xffff0000, v51
	v_pk_mul_f32 v[2:3], v[86:87], v[86:87]
	v_pk_fma_f32 v[2:3], v[88:89], v[88:89], v[2:3]
	v_pk_fma_f32 v[2:3], v[90:91], v[90:91], v[2:3]
	v_pk_fma_f32 v[2:3], v[92:93], v[92:93], v[2:3]
	v_pk_fma_f32 v[2:3], v[94:95], v[94:95], v[2:3]
	v_pk_fma_f32 v[2:3], v[96:97], v[96:97], v[2:3]
	v_pk_fma_f32 v[2:3], v[98:99], v[98:99], v[2:3]
	v_pk_fma_f32 v[2:3], v[100:101], v[100:101], v[2:3]
	v_pk_fma_f32 v[2:3], v[102:103], v[102:103], v[2:3]
	v_pk_fma_f32 v[2:3], v[104:105], v[104:105], v[2:3]
	v_pk_fma_f32 v[2:3], v[106:107], v[106:107], v[2:3]
	v_pk_fma_f32 v[2:3], v[108:109], v[108:109], v[2:3]
	v_pk_fma_f32 v[2:3], v[110:111], v[110:111], v[2:3]
	v_pk_fma_f32 v[2:3], v[112:113], v[112:113], v[2:3]
	v_pk_fma_f32 v[2:3], v[114:115], v[114:115], v[2:3]
	v_pk_fma_f32 v[2:3], v[116:117], v[116:117], v[2:3]
	v_add_f32_e32 v2, v2, v3
	ds_bpermute_b32 v3, v63, v2
	s_waitcnt lgkmcnt(0)
	v_add_f32_e32 v2, v2, v3
	ds_bpermute_b32 v3, v64, v2
	s_waitcnt lgkmcnt(0)
	v_add_f32_e32 v2, v2, v3
	ds_bpermute_b32 v3, v65, v2
	s_waitcnt lgkmcnt(0)
	v_add_f32_e32 v2, v2, v3
	ds_bpermute_b32 v3, v66, v2
	s_waitcnt lgkmcnt(0)
	v_add_f32_e32 v2, v2, v3
	ds_bpermute_b32 v3, v67, v2
	s_waitcnt lgkmcnt(0)
	v_add_f32_e32 v2, v2, v3
	ds_bpermute_b32 v3, v68, v2
	s_waitcnt lgkmcnt(0)
	v_add_f32_e32 v2, v2, v3
	v_mul_f32_e32 v2, 0x3a000000, v2
	v_add_f32_e32 v2, v73, v2
	v_rsq_f32_e32 v2, v2
	s_nop 0
	v_pk_mul_f32 v[86:87], v[86:87], v[2:3] op_sel_hi:[1,0]
	v_pk_mul_f32 v[88:89], v[88:89], v[2:3] op_sel_hi:[1,0]
	v_pk_mul_f32 v[90:91], v[90:91], v[2:3] op_sel_hi:[1,0]
	v_pk_mul_f32 v[92:93], v[92:93], v[2:3] op_sel_hi:[1,0]
	v_pk_mul_f32 v[94:95], v[94:95], v[2:3] op_sel_hi:[1,0]
	v_pk_mul_f32 v[96:97], v[96:97], v[2:3] op_sel_hi:[1,0]
	v_pk_mul_f32 v[98:99], v[98:99], v[2:3] op_sel_hi:[1,0]
	v_pk_mul_f32 v[100:101], v[100:101], v[2:3] op_sel_hi:[1,0]
	v_pk_mul_f32 v[102:103], v[102:103], v[2:3] op_sel_hi:[1,0]
	v_pk_mul_f32 v[104:105], v[104:105], v[2:3] op_sel_hi:[1,0]
	v_pk_mul_f32 v[106:107], v[106:107], v[2:3] op_sel_hi:[1,0]
	v_pk_mul_f32 v[108:109], v[108:109], v[2:3] op_sel_hi:[1,0]
	v_pk_mul_f32 v[110:111], v[110:111], v[2:3] op_sel_hi:[1,0]
	v_pk_mul_f32 v[112:113], v[112:113], v[2:3] op_sel_hi:[1,0]
	v_pk_mul_f32 v[114:115], v[114:115], v[2:3] op_sel_hi:[1,0]
	v_pk_mul_f32 v[116:117], v[116:117], v[2:3] op_sel_hi:[1,0]
	v_pk_fma_f32 v[86:87], v[86:87], v[160:161], v[192:193]
	v_pk_fma_f32 v[88:89], v[88:89], v[162:163], v[194:195]
	v_pk_fma_f32 v[90:91], v[90:91], v[164:165], v[196:197]
	v_pk_fma_f32 v[92:93], v[92:93], v[166:167], v[198:199]
	v_pk_fma_f32 v[94:95], v[94:95], v[168:169], v[200:201]
	v_pk_fma_f32 v[96:97], v[96:97], v[170:171], v[202:203]
	v_pk_fma_f32 v[98:99], v[98:99], v[172:173], v[204:205]
	v_pk_fma_f32 v[100:101], v[100:101], v[174:175], v[206:207]
	v_pk_fma_f32 v[102:103], v[102:103], v[176:177], v[208:209]
	v_pk_fma_f32 v[104:105], v[104:105], v[178:179], v[210:211]
	v_pk_fma_f32 v[106:107], v[106:107], v[180:181], v[212:213]
	v_pk_fma_f32 v[108:109], v[108:109], v[182:183], v[214:215]
	v_pk_fma_f32 v[110:111], v[110:111], v[184:185], v[216:217]
	v_pk_fma_f32 v[112:113], v[112:113], v[186:187], v[218:219]
	v_pk_fma_f32 v[114:115], v[114:115], v[188:189], v[220:221]
	v_pk_fma_f32 v[116:117], v[116:117], v[190:191], v[222:223]
	v_max_f32_e64 v4, |v86|, |v87|
	v_max3_f32 v4, |v88|, |v89|, v4
	v_max3_f32 v4, |v90|, |v91|, v4
	v_max3_f32 v4, |v92|, |v93|, v4
	v_max3_f32 v4, |v94|, |v95|, v4
	v_max3_f32 v4, |v96|, |v97|, v4
	v_max3_f32 v4, |v98|, |v99|, v4
	v_max3_f32 v4, |v100|, |v101|, v4
	v_max3_f32 v4, |v102|, |v103|, v4
	v_max3_f32 v4, |v104|, |v105|, v4
	v_max3_f32 v4, |v106|, |v107|, v4
	v_max3_f32 v4, |v108|, |v109|, v4
	v_max3_f32 v4, |v110|, |v111|, v4
	v_max3_f32 v4, |v112|, |v113|, v4
	v_max3_f32 v4, |v114|, |v115|, v4
	v_max3_f32 v4, |v116|, |v117|, v4
	ds_bpermute_b32 v5, v63, v4
	s_waitcnt lgkmcnt(0)
; #define LAS __attribute__((address_space(3)))
; __device__ __forceinline__ void phase_router(const Ctx& P, LAS unsigned char* lds, int vcu, int G) {
;     ...
;                 amax = fmaxf(amax, fmaxf(fmaxf(fabsf(h[0]), fabsf(h[1])), fmaxf(fabsf(h[2]), fabsf(h[3]))));
; #pragma unroll
;                 for (int e = 0; e < 8; ++e) { const f32x4 rw = *(const LAS f32x4*)(rwT + e * DM + c); lg[e] += (h[0] * rw[0] + h[1] * rw[1]) + (h[2] * rw[2] + h[3] * rw[3]); } }
; #pragma unroll
;             for (int e = 0; e < 8; ++e) lg[e] = wave_sum(lg[e]) + P.in[30][e];
; #pragma unroll
;             for (int o = 1; o < 64; o <<= 1) amax = fmaxf(amax, __shfl_xor(amax, o));
	v_max_f32_e32 v4, v4, v5
	ds_bpermute_b32 v5, v64, v4
	s_waitcnt lgkmcnt(0)
	v_max_f32_e32 v4, v4, v5
	ds_bpermute_b32 v5, v65, v4
	s_waitcnt lgkmcnt(0)
	v_max_f32_e32 v4, v4, v5
	ds_bpermute_b32 v5, v66, v4
	s_waitcnt lgkmcnt(0)
	v_max_f32_e32 v4, v4, v5
	ds_bpermute_b32 v5, v67, v4
	s_waitcnt lgkmcnt(0)
	v_max_f32_e32 v4, v4, v5
	ds_bpermute_b32 v5, v68, v4
	s_waitcnt lgkmcnt(0)
	v_max_f32_e32 v4, v4, v5
	v_max_f32_e32 v4, s77, v4
	ds_read_b128 v[134:137], v61 offset:0
	ds_read_b128 v[154:157], v61 offset:1024
	ds_read_b128 v[52:55], v61 offset:2048
	ds_read_b128 v[6:9], v61 offset:3072
	s_waitcnt lgkmcnt(3)
	v_pk_mul_f32 v[118:119], v[86:87], v[134:135]
	v_pk_fma_f32 v[118:119], v[88:89], v[136:137], v[118:119]
	ds_read_b128 v[134:137], v61 offset:4096
	s_waitcnt lgkmcnt(3)
	v_pk_fma_f32 v[118:119], v[90:91], v[154:155], v[118:119]
	v_pk_fma_f32 v[118:119], v[92:93], v[156:157], v[118:119]
	ds_read_b128 v[154:157], v61 offset:5120
	s_waitcnt lgkmcnt(3)
	v_pk_fma_f32 v[118:119], v[94:95], v[52:53], v[118:119]
	v_pk_fma_f32 v[118:119], v[96:97], v[54:55], v[118:119]
	ds_read_b128 v[52:55], v61 offset:6144
	s_waitcnt lgkmcnt(3)
	v_pk_fma_f32 v[118:119], v[98:99], v[6:7], v[118:119]
	v_pk_fma_f32 v[118:119], v[100:101], v[8:9], v[118:119]
	ds_read_b128 v[6:9], v61 offset:7168
	s_waitcnt lgkmcnt(3)
	v_pk_fma_f32 v[118:119], v[102:103], v[134:135], v[118:119]
	v_pk_fma_f32 v[118:119], v[104:105], v[136:137], v[118:119]
	ds_read_b128 v[134:137], v61 offset:8192
	s_waitcnt lgkmcnt(3)
	v_pk_fma_f32 v[118:119], v[106:107], v[154:155], v[118:119]
	v_pk_fma_f32 v[118:119], v[108:109], v[156:157], v[118:119]
	ds_read_b128 v[154:157], v61 offset:9216
	s_waitcnt lgkmcnt(3)
	v_pk_fma_f32 v[118:119], v[110:111], v[52:53], v[118:119]
	v_pk_fma_f32 v[118:119], v[112:113], v[54:55], v[118:119]
	ds_read_b128 v[52:55], v61 offset:10240
	s_waitcnt lgkmcnt(3)
	v_pk_fma_f32 v[118:119], v[114:115], v[6:7], v[118:119]
	v_pk_fma_f32 v[118:119], v[116:117], v[8:9], v[118:119]
	ds_read_b128 v[6:9], v61 offset:11264
	s_waitcnt lgkmcnt(3)
	v_pk_mul_f32 v[120:121], v[86:87], v[134:135]
	v_pk_fma_f32 v[120:121], v[88:89], v[136:137], v[120:121]
	ds_read_b128 v[134:137], v61 offset:12288
	s_waitcnt lgkmcnt(3)
	v_pk_fma_f32 v[120:121], v[90:91], v[154:155], v[120:121]
	v_pk_fma_f32 v[120:121], v[92:93], v[156:157], v[120:121]
	ds_read_b128 v[154:157], v61 offset:13312
	s_waitcnt lgkmcnt(3)
	v_pk_fma_f32 v[120:121], v[94:95], v[52:53], v[120:121]
	v_pk_fma_f32 v[120:121], v[96:97], v[54:55], v[120:121]
	ds_read_b128 v[52:55], v61 offset:14336
	s_waitcnt lgkmcnt(3)
	v_pk_fma_f32 v[120:121], v[98:99], v[6:7], v[120:121]
	v_pk_fma_f32 v[120:121], v[100:101], v[8:9], v[120:121]
	ds_read_b128 v[6:9], v61 offset:15360
	s_waitcnt lgkmcnt(3)
	v_pk_fma_f32 v[120:121], v[102:103], v[134:135], v[120:121]
	v_pk_fma_f32 v[120:121], v[104:105], v[136:137], v[120:121]
	ds_read_b128 v[134:137], v61 offset:16384
	s_waitcnt lgkmcnt(3)
	v_pk_fma_f32 v[120:121], v[106:107], v[154:155], v[120:121]
	v_pk_fma_f32 v[120:121], v[108:109], v[156:157], v[120:121]
	ds_read_b128 v[154:157], v61 offset:17408
	s_waitcnt lgkmcnt(3)
	v_pk_fma_f32 v[120:121], v[110:111], v[52:53], v[120:121]
	v_pk_fma_f32 v[120:121], v[112:113], v[54:55], v[120:121]
	ds_read_b128 v[52:55], v61 offset:18432
	s_waitcnt lgkmcnt(3)
	v_pk_fma_f32 v[120:121], v[114:115], v[6:7], v[120:121]
	v_pk_fma_f32 v[120:121], v[116:117], v[8:9], v[120:121]
	ds_read_b128 v[6:9], v61 offset:19456
	s_waitcnt lgkmcnt(3)
	v_pk_mul_f32 v[122:123], v[86:87], v[134:135]
	v_pk_fma_f32 v[122:123], v[88:89], v[136:137], v[122:123]
	ds_read_b128 v[134:137], v61 offset:20480
	s_waitcnt lgkmcnt(3)
	v_pk_fma_f32 v[122:123], v[90:91], v[154:155], v[122:123]
	v_pk_fma_f32 v[122:123], v[92:93], v[156:157], v[122:123]
	ds_read_b128 v[154:157], v61 offset:21504
	s_waitcnt lgkmcnt(3)
	v_pk_fma_f32 v[122:123], v[94:95], v[52:53], v[122:123]
	v_pk_fma_f32 v[122:123], v[96:97], v[54:55], v[122:123]
	ds_read_b128 v[52:55], v61 offset:22528
	s_waitcnt lgkmcnt(3)
	v_pk_fma_f32 v[122:123], v[98:99], v[6:7], v[122:123]
	v_pk_fma_f32 v[122:123], v[100:101], v[8:9], v[122:123]
	ds_read_b128 v[6:9], v61 offset:23552
	s_waitcnt lgkmcnt(3)
	v_pk_fma_f32 v[122:123], v[102:103], v[134:135], v[122:123]
	v_pk_fma_f32 v[122:123], v[104:105], v[136:137], v[122:123]
	ds_read_b128 v[134:137], v61 offset:24576
	s_waitcnt lgkmcnt(3)
	v_pk_fma_f32 v[122:123], v[106:107], v[154:155], v[122:123]
	v_pk_fma_f32 v[122:123], v[108:109], v[156:157], v[122:123]
	ds_read_b128 v[154:157], v61 offset:25600
	s_waitcnt lgkmcnt(3)
	v_pk_fma_f32 v[122:123], v[110:111], v[52:53], v[122:123]
	v_pk_fma_f32 v[122:123], v[112:113], v[54:55], v[122:123]
	ds_read_b128 v[52:55], v61 offset:26624
	s_waitcnt lgkmcnt(3)
	v_pk_fma_f32 v[122:123], v[114:115], v[6:7], v[122:123]
	v_pk_fma_f32 v[122:123], v[116:117], v[8:9], v[122:123]
	ds_read_b128 v[6:9], v61 offset:27648
	s_waitcnt lgkmcnt(3)
	v_pk_mul_f32 v[124:125], v[86:87], v[134:135]
	v_pk_fma_f32 v[124:125], v[88:89], v[136:137], v[124:125]
	ds_read_b128 v[134:137], v61 offset:28672
	s_waitcnt lgkmcnt(3)
	v_pk_fma_f32 v[124:125], v[90:91], v[154:155], v[124:125]
	v_pk_fma_f32 v[124:125], v[92:93], v[156:157], v[124:125]
	ds_read_b128 v[154:157], v61 offset:29696
	s_waitcnt lgkmcnt(3)
	v_pk_fma_f32 v[124:125], v[94:95], v[52:53], v[124:125]
	v_pk_fma_f32 v[124:125], v[96:97], v[54:55], v[124:125]
	ds_read_b128 v[52:55], v61 offset:30720
	s_waitcnt lgkmcnt(3)
	v_pk_fma_f32 v[124:125], v[98:99], v[6:7], v[124:125]
	v_pk_fma_f32 v[124:125], v[100:101], v[8:9], v[124:125]
	ds_read_b128 v[6:9], v61 offset:31744
	s_waitcnt lgkmcnt(3)
; #define LAS __attribute__((address_space(3)))
; __device__ __forceinline__ void phase_router(const Ctx& P, LAS unsigned char* lds, int vcu, int G) {
;     ...
; #pragma unroll
;             for (int j = 0; j < 8; ++j) { const int c = 4 * lane + 256 * j; const f32x4 g4 = *(const f32x4*)(gvec + c), sc4 = *(const f32x4*)(scp + c), sh4 = *(const f32x4*)(shp + c);
;                 const f32x4 h = v[j] * rstd * g4 * (sc4 + 1.0f) + sh4;
;                 amax = fmaxf(amax, fmaxf(fmaxf(fabsf(h[0]), fabsf(h[1])), fmaxf(fabsf(h[2]), fabsf(h[3]))));
; #pragma unroll
;                 for (int e = 0; e < 8; ++e) { const f32x4 rw = *(const LAS f32x4*)(rwT + e * DM + c); lg[e] += (h[0] * rw[0] + h[1] * rw[1]) + (h[2] * rw[2] + h[3] * rw[3]); } }
	v_pk_fma_f32 v[124:125], v[102:103], v[134:135], v[124:125]
	v_pk_fma_f32 v[124:125], v[104:105], v[136:137], v[124:125]
	ds_read_b128 v[134:137], v61 offset:32768
	s_waitcnt lgkmcnt(3)
	v_pk_fma_f32 v[124:125], v[106:107], v[154:155], v[124:125]
	v_pk_fma_f32 v[124:125], v[108:109], v[156:157], v[124:125]
	ds_read_b128 v[154:157], v61 offset:33792
	s_waitcnt lgkmcnt(3)
	v_pk_fma_f32 v[124:125], v[110:111], v[52:53], v[124:125]
	v_pk_fma_f32 v[124:125], v[112:113], v[54:55], v[124:125]
	ds_read_b128 v[52:55], v61 offset:34816
	s_waitcnt lgkmcnt(3)
	v_pk_fma_f32 v[124:125], v[114:115], v[6:7], v[124:125]
	v_pk_fma_f32 v[124:125], v[116:117], v[8:9], v[124:125]
	ds_read_b128 v[6:9], v61 offset:35840
	s_waitcnt lgkmcnt(3)
	v_pk_mul_f32 v[126:127], v[86:87], v[134:135]
	v_pk_fma_f32 v[126:127], v[88:89], v[136:137], v[126:127]
	ds_read_b128 v[134:137], v61 offset:36864
	s_waitcnt lgkmcnt(3)
	v_pk_fma_f32 v[126:127], v[90:91], v[154:155], v[126:127]
	v_pk_fma_f32 v[126:127], v[92:93], v[156:157], v[126:127]
	ds_read_b128 v[154:157], v61 offset:37888
	s_waitcnt lgkmcnt(3)
	v_pk_fma_f32 v[126:127], v[94:95], v[52:53], v[126:127]
	v_pk_fma_f32 v[126:127], v[96:97], v[54:55], v[126:127]
	ds_read_b128 v[52:55], v61 offset:38912
	s_waitcnt lgkmcnt(3)
	v_pk_fma_f32 v[126:127], v[98:99], v[6:7], v[126:127]
	v_pk_fma_f32 v[126:127], v[100:101], v[8:9], v[126:127]
	ds_read_b128 v[6:9], v61 offset:39936
	s_waitcnt lgkmcnt(3)
	v_pk_fma_f32 v[126:127], v[102:103], v[134:135], v[126:127]
	v_pk_fma_f32 v[126:127], v[104:105], v[136:137], v[126:127]
	ds_read_b128 v[134:137], v61 offset:40960
	s_waitcnt lgkmcnt(3)
	v_pk_fma_f32 v[126:127], v[106:107], v[154:155], v[126:127]
	v_pk_fma_f32 v[126:127], v[108:109], v[156:157], v[126:127]
	ds_read_b128 v[154:157], v61 offset:41984
	s_waitcnt lgkmcnt(3)
	v_pk_fma_f32 v[126:127], v[110:111], v[52:53], v[126:127]
	v_pk_fma_f32 v[126:127], v[112:113], v[54:55], v[126:127]
	ds_read_b128 v[52:55], v61 offset:43008
	s_waitcnt lgkmcnt(3)
	v_pk_fma_f32 v[126:127], v[114:115], v[6:7], v[126:127]
	v_pk_fma_f32 v[126:127], v[116:117], v[8:9], v[126:127]
	ds_read_b128 v[6:9], v61 offset:44032
	s_waitcnt lgkmcnt(3)
	v_pk_mul_f32 v[128:129], v[86:87], v[134:135]
	v_pk_fma_f32 v[128:129], v[88:89], v[136:137], v[128:129]
	ds_read_b128 v[134:137], v61 offset:45056
	s_waitcnt lgkmcnt(3)
	v_pk_fma_f32 v[128:129], v[90:91], v[154:155], v[128:129]
	v_pk_fma_f32 v[128:129], v[92:93], v[156:157], v[128:129]
	ds_read_b128 v[154:157], v61 offset:46080
	s_waitcnt lgkmcnt(3)
	v_pk_fma_f32 v[128:129], v[94:95], v[52:53], v[128:129]
	v_pk_fma_f32 v[128:129], v[96:97], v[54:55], v[128:129]
	ds_read_b128 v[52:55], v61 offset:47104
	s_waitcnt lgkmcnt(3)
	v_pk_fma_f32 v[128:129], v[98:99], v[6:7], v[128:129]
	v_pk_fma_f32 v[128:129], v[100:101], v[8:9], v[128:129]
	ds_read_b128 v[6:9], v61 offset:48128
	s_waitcnt lgkmcnt(3)
	v_pk_fma_f32 v[128:129], v[102:103], v[134:135], v[128:129]
	v_pk_fma_f32 v[128:129], v[104:105], v[136:137], v[128:129]
	ds_read_b128 v[134:137], v61 offset:49152
	s_waitcnt lgkmcnt(3)
	v_pk_fma_f32 v[128:129], v[106:107], v[154:155], v[128:129]
	v_pk_fma_f32 v[128:129], v[108:109], v[156:157], v[128:129]
	ds_read_b128 v[154:157], v61 offset:50176
	s_waitcnt lgkmcnt(3)
	v_pk_fma_f32 v[128:129], v[110:111], v[52:53], v[128:129]
	v_pk_fma_f32 v[128:129], v[112:113], v[54:55], v[128:129]
	ds_read_b128 v[52:55], v61 offset:51200
	s_waitcnt lgkmcnt(3)
	v_pk_fma_f32 v[128:129], v[114:115], v[6:7], v[128:129]
	v_pk_fma_f32 v[128:129], v[116:117], v[8:9], v[128:129]
	ds_read_b128 v[6:9], v61 offset:52224
	s_waitcnt lgkmcnt(3)
	v_pk_mul_f32 v[130:131], v[86:87], v[134:135]
	v_pk_fma_f32 v[130:131], v[88:89], v[136:137], v[130:131]
	ds_read_b128 v[134:137], v61 offset:53248
	s_waitcnt lgkmcnt(3)
	v_pk_fma_f32 v[130:131], v[90:91], v[154:155], v[130:131]
	v_pk_fma_f32 v[130:131], v[92:93], v[156:157], v[130:131]
	ds_read_b128 v[154:157], v61 offset:54272
	s_waitcnt lgkmcnt(3)
	v_pk_fma_f32 v[130:131], v[94:95], v[52:53], v[130:131]
	v_pk_fma_f32 v[130:131], v[96:97], v[54:55], v[130:131]
	ds_read_b128 v[52:55], v61 offset:55296
	s_waitcnt lgkmcnt(3)
	v_pk_fma_f32 v[130:131], v[98:99], v[6:7], v[130:131]
	v_pk_fma_f32 v[130:131], v[100:101], v[8:9], v[130:131]
	ds_read_b128 v[6:9], v61 offset:56320
	s_waitcnt lgkmcnt(3)
	v_pk_fma_f32 v[130:131], v[102:103], v[134:135], v[130:131]
	v_pk_fma_f32 v[130:131], v[104:105], v[136:137], v[130:131]
	ds_read_b128 v[134:137], v61 offset:57344
	s_waitcnt lgkmcnt(3)
	v_pk_fma_f32 v[130:131], v[106:107], v[154:155], v[130:131]
	v_pk_fma_f32 v[130:131], v[108:109], v[156:157], v[130:131]
	ds_read_b128 v[154:157], v61 offset:58368
	s_waitcnt lgkmcnt(3)
	v_pk_fma_f32 v[130:131], v[110:111], v[52:53], v[130:131]
	v_pk_fma_f32 v[130:131], v[112:113], v[54:55], v[130:131]
	ds_read_b128 v[52:55], v61 offset:59392
	s_waitcnt lgkmcnt(3)
	v_pk_fma_f32 v[130:131], v[114:115], v[6:7], v[130:131]
	v_pk_fma_f32 v[130:131], v[116:117], v[8:9], v[130:131]
	ds_read_b128 v[6:9], v61 offset:60416
	s_waitcnt lgkmcnt(3)
	v_pk_mul_f32 v[132:133], v[86:87], v[134:135]
	v_pk_fma_f32 v[132:133], v[88:89], v[136:137], v[132:133]
	ds_read_b128 v[134:137], v61 offset:61440
	s_waitcnt lgkmcnt(3)
	v_pk_fma_f32 v[132:133], v[90:91], v[154:155], v[132:133]
	v_pk_fma_f32 v[132:133], v[92:93], v[156:157], v[132:133]
	ds_read_b128 v[154:157], v61 offset:62464
	s_waitcnt lgkmcnt(3)
	v_pk_fma_f32 v[132:133], v[94:95], v[52:53], v[132:133]
	v_pk_fma_f32 v[132:133], v[96:97], v[54:55], v[132:133]
	ds_read_b128 v[52:55], v61 offset:63488
	s_waitcnt lgkmcnt(3)
; #define LAS __attribute__((address_space(3)))
; __device__ __forceinline__ f32x4 ld4_bf(const bf16_t* p) { const u32x2 w = *(const u32x2*)p; return (f32x4){bf_lo(w.x), bf_hi(w.x), bf_lo(w.y), bf_hi(w.y)}; }
; __device__ __forceinline__ void phase_router(const Ctx& P, LAS unsigned char* lds, int vcu, int G) {
;     ...
;                 for (int e = 0; e < 8; ++e) { const f32x4 rw = *(const LAS f32x4*)(rwT + e * DM + c); lg[e] += (h[0] * rw[0] + h[1] * rw[1]) + (h[2] * rw[2] + h[3] * rw[3]); } }
; #pragma unroll
;             for (int e = 0; e < 8; ++e) lg[e] = wave_sum(lg[e]) + P.in[30][e];
; #pragma unroll
;             for (int o = 1; o < 64; o <<= 1) amax = fmaxf(amax, __shfl_xor(amax, o));
;             amax = fmaxf(amax, 1e-30f);
;             if (lane == 0) rscl[lr] = amax * (1.0f / 127.0f);
;             { const float qs = 127.0f / amax; int l2 = lane; asm volatile("" : "+v"(l2));
; #pragma unroll 2
;               for (int j = 0; j < 8; ++j) { const int c = 4 * l2 + 256 * j; const f32x4 x4 = ld4_bf(xr + c), g4 = *(const f32x4*)(gvec + c), sc4 = *(const f32x4*)(scp + c), sh4 = *(const f32x4*)(shp + c);
;                   const f32x4 h = (x4 * rstd * g4 * (sc4 + 1.0f) + sh4) * qs; *(LAS unsigned*)(rows8 + lr * DM + c) = cvt4_i8(h[0], h[1], h[2], h[3]); } }
	v_pk_fma_f32 v[132:133], v[98:99], v[6:7], v[132:133]
	v_pk_fma_f32 v[132:133], v[100:101], v[8:9], v[132:133]
	ds_read_b128 v[6:9], v61 offset:64512
	s_waitcnt lgkmcnt(3)
	v_pk_fma_f32 v[132:133], v[102:103], v[134:135], v[132:133]
	v_pk_fma_f32 v[132:133], v[104:105], v[136:137], v[132:133]
	s_waitcnt lgkmcnt(2)
	v_pk_fma_f32 v[132:133], v[106:107], v[154:155], v[132:133]
	v_pk_fma_f32 v[132:133], v[108:109], v[156:157], v[132:133]
	s_waitcnt lgkmcnt(1)
	v_pk_fma_f32 v[132:133], v[110:111], v[52:53], v[132:133]
	v_pk_fma_f32 v[132:133], v[112:113], v[54:55], v[132:133]
	s_waitcnt lgkmcnt(0)
	v_pk_fma_f32 v[132:133], v[114:115], v[6:7], v[132:133]
	v_pk_fma_f32 v[132:133], v[116:117], v[8:9], v[132:133]
	v_add_f32_e32 v118, v118, v119
	v_add_f32_e32 v120, v120, v121
	v_add_f32_e32 v122, v122, v123
	v_add_f32_e32 v124, v124, v125
	v_add_f32_e32 v126, v126, v127
	v_add_f32_e32 v128, v128, v129
	v_add_f32_e32 v130, v130, v131
	v_add_f32_e32 v132, v132, v133
	ds_bpermute_b32 v36, v63, v118
	ds_bpermute_b32 v37, v63, v120
	ds_bpermute_b32 v38, v63, v122
	ds_bpermute_b32 v39, v63, v124
	ds_bpermute_b32 v40, v63, v126
	ds_bpermute_b32 v41, v63, v128
	ds_bpermute_b32 v42, v63, v130
	ds_bpermute_b32 v43, v63, v132
	s_waitcnt lgkmcnt(0)
	v_add_f32_e32 v118, v118, v36
	v_add_f32_e32 v120, v120, v37
	v_add_f32_e32 v122, v122, v38
	v_add_f32_e32 v124, v124, v39
	v_add_f32_e32 v126, v126, v40
	v_add_f32_e32 v128, v128, v41
	v_add_f32_e32 v130, v130, v42
	v_add_f32_e32 v132, v132, v43
	ds_bpermute_b32 v36, v64, v118
	ds_bpermute_b32 v37, v64, v120
	ds_bpermute_b32 v38, v64, v122
	ds_bpermute_b32 v39, v64, v124
	ds_bpermute_b32 v40, v64, v126
	ds_bpermute_b32 v41, v64, v128
	ds_bpermute_b32 v42, v64, v130
	ds_bpermute_b32 v43, v64, v132
	s_waitcnt lgkmcnt(0)
	v_add_f32_e32 v118, v118, v36
	v_add_f32_e32 v120, v120, v37
	v_add_f32_e32 v122, v122, v38
	v_add_f32_e32 v124, v124, v39
	v_add_f32_e32 v126, v126, v40
	v_add_f32_e32 v128, v128, v41
	v_add_f32_e32 v130, v130, v42
	v_add_f32_e32 v132, v132, v43
	ds_bpermute_b32 v36, v65, v118
	ds_bpermute_b32 v37, v65, v120
	ds_bpermute_b32 v38, v65, v122
	ds_bpermute_b32 v39, v65, v124
	ds_bpermute_b32 v40, v65, v126
	ds_bpermute_b32 v41, v65, v128
	ds_bpermute_b32 v42, v65, v130
	ds_bpermute_b32 v43, v65, v132
	s_waitcnt lgkmcnt(0)
	v_add_f32_e32 v118, v118, v36
	v_add_f32_e32 v120, v120, v37
	v_add_f32_e32 v122, v122, v38
	v_add_f32_e32 v124, v124, v39
	v_add_f32_e32 v126, v126, v40
	v_add_f32_e32 v128, v128, v41
	v_add_f32_e32 v130, v130, v42
	v_add_f32_e32 v132, v132, v43
	ds_bpermute_b32 v36, v66, v118
	ds_bpermute_b32 v37, v66, v120
	ds_bpermute_b32 v38, v66, v122
	ds_bpermute_b32 v39, v66, v124
	ds_bpermute_b32 v40, v66, v126
	ds_bpermute_b32 v41, v66, v128
	ds_bpermute_b32 v42, v66, v130
	ds_bpermute_b32 v43, v66, v132
	s_waitcnt lgkmcnt(0)
	v_add_f32_e32 v118, v118, v36
	v_add_f32_e32 v120, v120, v37
	v_add_f32_e32 v122, v122, v38
	v_add_f32_e32 v124, v124, v39
	v_add_f32_e32 v126, v126, v40
	v_add_f32_e32 v128, v128, v41
	v_add_f32_e32 v130, v130, v42
	v_add_f32_e32 v132, v132, v43
	ds_bpermute_b32 v36, v67, v118
	ds_bpermute_b32 v37, v67, v120
	ds_bpermute_b32 v38, v67, v122
	ds_bpermute_b32 v39, v67, v124
	ds_bpermute_b32 v40, v67, v126
	ds_bpermute_b32 v41, v67, v128
	ds_bpermute_b32 v42, v67, v130
	ds_bpermute_b32 v43, v67, v132
	s_waitcnt lgkmcnt(0)
	v_add_f32_e32 v118, v118, v36
	v_add_f32_e32 v120, v120, v37
	v_add_f32_e32 v122, v122, v38
	v_add_f32_e32 v124, v124, v39
	v_add_f32_e32 v126, v126, v40
	v_add_f32_e32 v128, v128, v41
	v_add_f32_e32 v130, v130, v42
	v_add_f32_e32 v132, v132, v43
	ds_bpermute_b32 v36, v68, v118
	ds_bpermute_b32 v37, v68, v120
	ds_bpermute_b32 v38, v68, v122
	ds_bpermute_b32 v39, v68, v124
	ds_bpermute_b32 v40, v68, v126
	ds_bpermute_b32 v41, v68, v128
	ds_bpermute_b32 v42, v68, v130
	ds_bpermute_b32 v43, v68, v132
	s_waitcnt lgkmcnt(0)
	v_add_f32_e32 v118, v118, v36
	v_add_f32_e32 v120, v120, v37
	v_add_f32_e32 v122, v122, v38
	v_add_f32_e32 v124, v124, v39
	v_add_f32_e32 v126, v126, v40
	v_add_f32_e32 v128, v128, v41
	v_add_f32_e32 v130, v130, v42
	v_add_f32_e32 v132, v132, v43
	v_add_f32_e32 v118, v224, v118
	v_add_f32_e32 v120, v225, v120
	v_add_f32_e32 v122, v226, v122
	v_add_f32_e32 v124, v227, v124
	v_add_f32_e32 v126, v228, v126
	v_add_f32_e32 v128, v229, v128
	v_add_f32_e32 v130, v230, v130
	v_add_f32_e32 v132, v231, v132
	s_and_saveexec_b64 s[14:15], s[4:5]
	v_mul_f32_e32 v5, 0x3c010204, v4
	s_lshl_b32 s18, s86, 2
	s_add_i32 s18, s18, 0x20760
	v_mov_b32_e32 v6, s18
	ds_write_b32 v6, v5
	s_or_b64 exec, exec, s[14:15]
	v_rcp_f32_e32 v6, v4
	v_mov_b32_e32 v8, 0x4b400000
	v_mul_f32_e32 v6, s78, v6
	v_pk_mul_f32 v[86:87], v[86:87], v[6:7] op_sel_hi:[1,0]
	v_pk_mul_f32 v[88:89], v[88:89], v[6:7] op_sel_hi:[1,0]
	v_pk_add_f32 v[86:87], v[86:87], v[8:9] op_sel_hi:[1,0]
	v_pk_add_f32 v[88:89], v[88:89], v[8:9] op_sel_hi:[1,0]
	v_med3_f32 v86, v86, s79, v83
	v_med3_f32 v87, v87, s79, v83
	v_med3_f32 v88, v88, s79, v83
	v_med3_f32 v89, v89, s79, v83
	v_perm_b32 v86, v87, v86, s80
	v_perm_b32 v88, v89, v88, s80
	v_perm_b32 v86, v88, v86, s81
	ds_write_b32 v35, v86
	v_pk_mul_f32 v[90:91], v[90:91], v[6:7] op_sel_hi:[1,0]
	v_pk_mul_f32 v[92:93], v[92:93], v[6:7] op_sel_hi:[1,0]
	v_pk_add_f32 v[90:91], v[90:91], v[8:9] op_sel_hi:[1,0]
	v_pk_add_f32 v[92:93], v[92:93], v[8:9] op_sel_hi:[1,0]
	v_med3_f32 v90, v90, s79, v83
	v_med3_f32 v91, v91, s79, v83
	v_med3_f32 v92, v92, s79, v83
	v_med3_f32 v93, v93, s79, v83
	v_perm_b32 v90, v91, v90, s80
	v_perm_b32 v92, v93, v92, s80
	v_perm_b32 v90, v92, v90, s81
	ds_write_b32 v35, v90 offset:256
	v_pk_mul_f32 v[94:95], v[94:95], v[6:7] op_sel_hi:[1,0]
; #define LAS __attribute__((address_space(3)))
; __device__ __forceinline__ f32x4 ld4_bf(const bf16_t* p) { const u32x2 w = *(const u32x2*)p; return (f32x4){bf_lo(w.x), bf_hi(w.x), bf_lo(w.y), bf_hi(w.y)}; }
; __device__ __forceinline__ void phase_router(const Ctx& P, LAS unsigned char* lds, int vcu, int G) {
;     ...
;             { const float qs = 127.0f / amax; int l2 = lane; asm volatile("" : "+v"(l2));
; #pragma unroll 2
;               for (int j = 0; j < 8; ++j) { const int c = 4 * l2 + 256 * j; const f32x4 x4 = ld4_bf(xr + c), g4 = *(const f32x4*)(gvec + c), sc4 = *(const f32x4*)(scp + c), sh4 = *(const f32x4*)(shp + c);
;                   const f32x4 h = (x4 * rstd * g4 * (sc4 + 1.0f) + sh4) * qs; *(LAS unsigned*)(rows8 + lr * DM + c) = cvt4_i8(h[0], h[1], h[2], h[3]); } }
;             int i1 = 0; float v1 = lg[0];
; #pragma unroll
;             for (int e = 1; e < 8; ++e) if (lg[e] > v1) { v1 = lg[e]; i1 = e; }
;             int i2 = -1; float v2 = -3.0e38f;
; #pragma unroll
;             for (int e = 0; e < 8; ++e) if (e != i1 && lg[e] > v2) { v2 = lg[e]; i2 = e; }
;             const float p1 = 1.0f / (1.0f + __expf(v2 - v1));
;             if (lane == 0) { sel[lr * 2] = i1; sel[lr * 2 + 1] = i2; prb[lr * 2] = p1; prb[lr * 2 + 1] = 1.0f - p1; }
	v_pk_mul_f32 v[96:97], v[96:97], v[6:7] op_sel_hi:[1,0]
	v_pk_add_f32 v[94:95], v[94:95], v[8:9] op_sel_hi:[1,0]
	v_pk_add_f32 v[96:97], v[96:97], v[8:9] op_sel_hi:[1,0]
	v_med3_f32 v94, v94, s79, v83
	v_med3_f32 v95, v95, s79, v83
	v_med3_f32 v96, v96, s79, v83
	v_med3_f32 v97, v97, s79, v83
	v_perm_b32 v94, v95, v94, s80
	v_perm_b32 v96, v97, v96, s80
	v_perm_b32 v94, v96, v94, s81
	ds_write_b32 v35, v94 offset:512
	v_pk_mul_f32 v[98:99], v[98:99], v[6:7] op_sel_hi:[1,0]
	v_pk_mul_f32 v[100:101], v[100:101], v[6:7] op_sel_hi:[1,0]
	v_pk_add_f32 v[98:99], v[98:99], v[8:9] op_sel_hi:[1,0]
	v_pk_add_f32 v[100:101], v[100:101], v[8:9] op_sel_hi:[1,0]
	v_med3_f32 v98, v98, s79, v83
	v_med3_f32 v99, v99, s79, v83
	v_med3_f32 v100, v100, s79, v83
	v_med3_f32 v101, v101, s79, v83
	v_perm_b32 v98, v99, v98, s80
	v_perm_b32 v100, v101, v100, s80
	v_perm_b32 v98, v100, v98, s81
	ds_write_b32 v35, v98 offset:768
	v_pk_mul_f32 v[102:103], v[102:103], v[6:7] op_sel_hi:[1,0]
	v_pk_mul_f32 v[104:105], v[104:105], v[6:7] op_sel_hi:[1,0]
	v_pk_add_f32 v[102:103], v[102:103], v[8:9] op_sel_hi:[1,0]
	v_pk_add_f32 v[104:105], v[104:105], v[8:9] op_sel_hi:[1,0]
	v_med3_f32 v102, v102, s79, v83
	v_med3_f32 v103, v103, s79, v83
	v_med3_f32 v104, v104, s79, v83
	v_med3_f32 v105, v105, s79, v83
	v_perm_b32 v102, v103, v102, s80
	v_perm_b32 v104, v105, v104, s80
	v_perm_b32 v102, v104, v102, s81
	ds_write_b32 v35, v102 offset:1024
	v_pk_mul_f32 v[106:107], v[106:107], v[6:7] op_sel_hi:[1,0]
	v_pk_mul_f32 v[108:109], v[108:109], v[6:7] op_sel_hi:[1,0]
	v_pk_add_f32 v[106:107], v[106:107], v[8:9] op_sel_hi:[1,0]
	v_pk_add_f32 v[108:109], v[108:109], v[8:9] op_sel_hi:[1,0]
	v_med3_f32 v106, v106, s79, v83
	v_med3_f32 v107, v107, s79, v83
	v_med3_f32 v108, v108, s79, v83
	v_med3_f32 v109, v109, s79, v83
	v_perm_b32 v106, v107, v106, s80
	v_perm_b32 v108, v109, v108, s80
	v_perm_b32 v106, v108, v106, s81
	ds_write_b32 v35, v106 offset:1280
	v_pk_mul_f32 v[110:111], v[110:111], v[6:7] op_sel_hi:[1,0]
	v_pk_mul_f32 v[112:113], v[112:113], v[6:7] op_sel_hi:[1,0]
	v_pk_add_f32 v[110:111], v[110:111], v[8:9] op_sel_hi:[1,0]
	v_pk_add_f32 v[112:113], v[112:113], v[8:9] op_sel_hi:[1,0]
	v_med3_f32 v110, v110, s79, v83
	v_med3_f32 v111, v111, s79, v83
	v_med3_f32 v112, v112, s79, v83
	v_med3_f32 v113, v113, s79, v83
	v_perm_b32 v110, v111, v110, s80
	v_perm_b32 v112, v113, v112, s80
	v_perm_b32 v110, v112, v110, s81
	ds_write_b32 v35, v110 offset:1536
	v_pk_mul_f32 v[114:115], v[114:115], v[6:7] op_sel_hi:[1,0]
	v_pk_mul_f32 v[116:117], v[116:117], v[6:7] op_sel_hi:[1,0]
	v_pk_add_f32 v[114:115], v[114:115], v[8:9] op_sel_hi:[1,0]
	v_pk_add_f32 v[116:117], v[116:117], v[8:9] op_sel_hi:[1,0]
	v_med3_f32 v114, v114, s79, v83
	v_med3_f32 v115, v115, s79, v83
	v_med3_f32 v116, v116, s79, v83
	v_med3_f32 v117, v117, s79, v83
	v_perm_b32 v114, v115, v114, s80
	v_perm_b32 v116, v117, v116, s80
	v_perm_b32 v114, v116, v114, s81
	ds_write_b32 v35, v114 offset:1792
	v_mov_b32_e32 v44, 0
	v_mov_b32_e32 v45, v118
	v_cmp_gt_f32_e32 vcc, v120, v45
	s_nop 1
	v_cndmask_b32_e32 v45, v45, v120, vcc
	v_cndmask_b32_e64 v44, v44, 1, vcc
	v_cmp_gt_f32_e32 vcc, v122, v45
	s_nop 1
	v_cndmask_b32_e32 v45, v45, v122, vcc
	v_cndmask_b32_e64 v44, v44, 2, vcc
	v_cmp_gt_f32_e32 vcc, v124, v45
	s_nop 1
	v_cndmask_b32_e32 v45, v45, v124, vcc
	v_cndmask_b32_e64 v44, v44, 3, vcc
	v_cmp_gt_f32_e32 vcc, v126, v45
	s_nop 1
	v_cndmask_b32_e32 v45, v45, v126, vcc
	v_cndmask_b32_e64 v44, v44, 4, vcc
	v_cmp_gt_f32_e32 vcc, v128, v45
	s_nop 1
	v_cndmask_b32_e32 v45, v45, v128, vcc
	v_cndmask_b32_e64 v44, v44, 5, vcc
	v_cmp_gt_f32_e32 vcc, v130, v45
	s_nop 1
	v_cndmask_b32_e32 v45, v45, v130, vcc
	v_cndmask_b32_e64 v44, v44, 6, vcc
	v_cmp_gt_f32_e32 vcc, v132, v45
	s_nop 1
	v_cndmask_b32_e32 v45, v45, v132, vcc
	v_cndmask_b32_e64 v44, v44, 7, vcc
	v_mov_b32_e32 v46, -1
	v_mov_b32_e32 v47, v84
	v_cmp_ne_u32_e64 s[16:17], 0, v44
	v_cmp_gt_f32_e32 vcc, v118, v47
	s_and_b64 vcc, vcc, s[16:17]
	s_nop 1
	v_cndmask_b32_e32 v47, v47, v118, vcc
	v_cndmask_b32_e64 v46, v46, 0, vcc
	v_cmp_ne_u32_e64 s[16:17], 1, v44
	v_cmp_gt_f32_e32 vcc, v120, v47
	s_and_b64 vcc, vcc, s[16:17]
	s_nop 1
	v_cndmask_b32_e32 v47, v47, v120, vcc
	v_cndmask_b32_e64 v46, v46, 1, vcc
	v_cmp_ne_u32_e64 s[16:17], 2, v44
	v_cmp_gt_f32_e32 vcc, v122, v47
	s_and_b64 vcc, vcc, s[16:17]
	s_nop 1
	v_cndmask_b32_e32 v47, v47, v122, vcc
	v_cndmask_b32_e64 v46, v46, 2, vcc
	v_cmp_ne_u32_e64 s[16:17], 3, v44
	v_cmp_gt_f32_e32 vcc, v124, v47
	s_and_b64 vcc, vcc, s[16:17]
	s_nop 1
	v_cndmask_b32_e32 v47, v47, v124, vcc
	v_cndmask_b32_e64 v46, v46, 3, vcc
	v_cmp_ne_u32_e64 s[16:17], 4, v44
	v_cmp_gt_f32_e32 vcc, v126, v47
	s_and_b64 vcc, vcc, s[16:17]
	s_nop 1
	v_cndmask_b32_e32 v47, v47, v126, vcc
	v_cndmask_b32_e64 v46, v46, 4, vcc
	v_cmp_ne_u32_e64 s[16:17], 5, v44
	v_cmp_gt_f32_e32 vcc, v128, v47
	s_and_b64 vcc, vcc, s[16:17]
	s_nop 1
	v_cndmask_b32_e32 v47, v47, v128, vcc
	v_cndmask_b32_e64 v46, v46, 5, vcc
	v_cmp_ne_u32_e64 s[16:17], 6, v44
	v_cmp_gt_f32_e32 vcc, v130, v47
	s_and_b64 vcc, vcc, s[16:17]
	s_nop 1
	v_cndmask_b32_e32 v47, v47, v130, vcc
	v_cndmask_b32_e64 v46, v46, 6, vcc
	v_cmp_ne_u32_e64 s[16:17], 7, v44
	v_cmp_gt_f32_e32 vcc, v132, v47
	s_and_b64 vcc, vcc, s[16:17]
	s_nop 1
	v_cndmask_b32_e32 v47, v47, v132, vcc
	v_cndmask_b32_e64 v46, v46, 7, vcc
	v_sub_f32_e32 v48, v47, v45
	v_mul_f32_e32 v48, 0x3fb8aa3b, v48
	v_exp_f32_e32 v48, v48
	s_nop 0
	v_add_f32_e32 v48, 1.0, v48
	v_rcp_f32_e32 v48, v48
	s_nop 0
	v_sub_f32_e32 v49, 1.0, v48
	v_mov_b32_e32 v45, v46
	s_and_saveexec_b64 s[44:45], s[4:5]
	s_lshl_b32 s10, s86, 3
	s_add_i32 s11, s10, 0x20400
	v_mov_b32_e32 v5, s11
	s_add_i32 s10, s10, 0x20500
	ds_write_b64 v5, v[44:45]
	v_mov_b32_e32 v2, s10
	ds_write_b64 v2, v[48:49]
	s_branch .LBB0_2348
